# baseline (speedup 1.0000x reference)
_Z8gemm_qkvPKDF16_S0_PKfS2_S2_PDF16_S3_S3_:
	s_load_dwordx8 s[12:19], s[0:1], 0x0
	s_load_dwordx8 s[4:11], s[0:1], 0x20
	s_mov_b32 s66, s2
	s_bitcmp0_b32 s2, 5
	s_mov_b64 s[0:1], -1
	s_cbranch_scc0 .LBB1_3
	s_and_b64 vcc, exec, s[0:1]
	s_cbranch_vccnz .LBB1_60
